# speedup vs baseline: 1.0177x; 1.0177x over previous
.Lk_291:
	s_or_b64 exec, exec, s[12:13]
	v_add_f32_e32 v216, 1.0, v52
	v_add_f32_e32 v217, 1.0, v50
	v_lshlrev_b32_e32 v215, 9, v177
	v_cmp_neq_f32_e32 vcc, 0, v216
	v_and_b32_e32 v215, 0x1e00, v215
	v_or_b32_e32 v250, v215, v160
	v_cndmask_b32_e32 v216, v173, v216, vcc
	v_cmp_neq_f32_e32 vcc, 0, v217
	v_or_b32_e32 v251, v215, v164
	v_lshlrev_b32_e32 v250, 3, v250
	v_cndmask_b32_e32 v217, v173, v217, vcc
	v_lshlrev_b32_e32 v251, 3, v251
	s_waitcnt vmcnt(0)
	v_mov_b32_e32 v64, v182
	v_mov_b32_e32 v46, v183
	s_mov_b32 s90, 0
	s_xor_b64 s[50:51], s[44:45], -1
	v_add_u32_e32 v12, 1, v177
	s_mov_b64 s[12:13], -1
	s_and_saveexec_b64 s[48:49], s[50:51]
	s_cbranch_execz .Lk_303
.Lmy_rx_chk:
	v_lshrrev_b32_e32 v65, 20, v64
	v_cmp_eq_u32_e32 vcc, v65, v12
	v_lshrrev_b32_e32 v65, 20, v46
	v_cmp_eq_u32_e64 s[12:13], v65, v12
	s_and_b64 s[12:13], vcc, s[12:13]
	s_nop 0
	v_cndmask_b32_e64 v65, 0, 1, s[12:13]
	v_cmp_ne_u32_e32 vcc, 0, v65
	s_cmp_eq_u64 vcc, exec
	s_mov_b64 s[12:13], 0
	s_cbranch_scc1 .Lk_302
	s_cmp_eq_u32 s90, 0
	s_cbranch_scc0 .Lmy_rx_spin
	s_mov_b32 s90, 1
	global_load_dword v184, v213, s[66:67] sc1
	global_load_dword v185, v214, s[66:67] sc1
	v_lshlrev_b32_e32 v72, 13, v177
	v_and_b32_e32 v72, 0x6000, v72
	v_add_u32_e32 v65, v72, v166
	v_add_u32_e32 v72, v72, v165
	v_mov_b32_e32 v73, 0
	v_lshlrev_b64 v[56:57], 7, v[72:73]
	v_mov_b32_e32 v72, v65
	v_lshl_add_u64 v[56:57], s[66:67], 0, v[56:57]
	v_lshlrev_b64 v[60:61], 7, v[72:73]
	v_mov_b32_e32 v72, v213
	v_lshl_add_u64 v[60:61], s[66:67], 0, v[60:61]
	v_lshl_add_u64 v[58:59], s[66:67], 0, v[72:73]
	v_mov_b32_e32 v72, v214
	s_nop 0
	v_lshl_add_u64 v[62:63], s[66:67], 0, v[72:73]
	s_waitcnt vmcnt(0)
	v_mov_b32_e32 v64, v184
	v_mov_b32_e32 v46, v185
	s_branch .Lmy_rx_chk
.Lmy_rx_spin:
	s_cmp_eq_u64 s[10:11], 0
	s_cselect_b32 s89, 0xff, 3
	s_mov_b32 s60, 0
